# P3 phase: each wave loads only its quarter of the S fragments and shares them through LDS (cuts per-CU global requests 4x)
# speedup vs baseline: 1.1131x; 1.0009x over previous
.LBB0_959:
	s_andn2_b64 vcc, exec, s[0:1]
	s_cbranch_vccnz .LBB0_1015
	s_mov_b64 s[4:5], s[46:47]
	s_waitcnt vmcnt(0)
	v_mbcnt_lo_u32_b32 v0, -1, 0
	v_mbcnt_hi_u32_b32 v0, -1, v0
	v_readlane_b32 s0, v254, 62
	v_add_u32_e32 v0, s3, v0
	v_readlane_b32 s1, v254, 63
	s_andn2_b64 vcc, exec, s[0:1]
	v_readfirstlane_b32 s2, v0
	s_cbranch_vccnz .LBB0_963
	s_load_dwordx2 s[0:1], s[4:5], 0xd8
	s_nop 0
	s_load_dwordx2 s[4:5], s[4:5], 0x58
	v_and_b32_e32 v1, 15, v0
	v_bfe_u32 v9, v0, 4, 2
	v_lshlrev_b32_e32 v2, 4, v9
	s_waitcnt lgkmcnt(0)
	s_add_u32 s28, s0, 0x1eaac000
	s_addc_u32 s29, s1, 0
	s_lshl_b32 s74, s11, 7
	s_lshl_b64 s[8:9], s[74:75], 2
	s_add_u32 s4, s4, s8
	s_addc_u32 s5, s5, s9
	s_ashr_i32 s7, s2, 8
	s_lshr_b32 s2, s2, 2
	v_and_or_b32 v146, s2, 48, v1
	v_lshlrev_b32_e32 v96, 8, v146
	v_mov_b32_e32 v3, v97
	v_lshl_add_u64 v[4:5], s[0:1], 0, v[96:97]
	v_lshl_add_u64 v[6:7], v[4:5], 0, v[2:3]
	s_mov_b64 s[8:9], 0x482ac000
	v_lshlrev_b32_e32 v1, 3, v0
	v_and_b32_e32 v0, 3, v0
	s_movk_i32 s2, 0x60
	v_lshl_add_u64 v[148:149], v[6:7], 0, s[8:9]
	v_and_or_b32 v6, v1, s2, v0
	s_load_dword s2, s[62:63], 0x0
	v_lshl_add_u64 v[0:1], s[0:1], 0, v[2:3]
	s_mov_b64 s[8:9], 0x502ac000
	v_lshlrev_b32_e32 v96, 6, v9
	v_lshl_add_u64 v[150:151], v[0:1], 0, s[8:9]
	v_lshl_add_u64 v[2:3], v[4:5], 0, v[96:97]
	s_mov_b64 s[8:9], 0x4c2ac000
	v_lshlrev_b32_e32 v96, 7, v9
	v_lshl_add_u64 v[152:153], v[2:3], 0, s[8:9]
	v_lshlrev_b32_e32 v2, 7, v6
	v_lshl_add_u64 v[154:155], s[4:5], 0, v[96:97]
	v_readlane_b32 s4, v254, 57
	v_lshlrev_b32_e32 v0, 5, v9
	v_or_b32_e32 v4, 0x800, v2
	v_or_b32_e32 v6, 0xa00, v2
	v_or_b32_e32 v8, 0xc00, v2
	v_or_b32_e32 v10, 0xe00, v2
	s_add_i32 s30, s4, s7
	s_lshl_b32 s5, s7, 6
	v_readlane_b32 s7, v255, 18
	s_waitcnt lgkmcnt(0)
	s_lshl_b32 s4, s2, 1
	s_add_i32 s5, s7, s5
	s_lshl_b32 s7, s2, 7
	v_lshlrev_b32_e32 v96, 1, v2
	v_lshlrev_b32_e32 v156, 1, v4
	v_lshlrev_b32_e32 v158, 1, v6
	v_lshlrev_b32_e32 v160, 1, v8
	v_lshlrev_b32_e32 v174, 1, v10
	v_lshlrev_b32_e32 v176, 1, v0
	s_mov_b32 s8, s94
	s_lshr_b32 s14, s3, 6
	s_and_b32 s15, s14, 3
	s_lshr_b32 s14, s14, 2
	s_lshl_b32 s14, s14, 15
	v_mbcnt_lo_u32_b32 v235, -1, 0
	v_mbcnt_hi_u32_b32 v235, -1, v235
	v_lshlrev_b32_e32 v235, 4, v235
	v_add_u32_e32 v235, s14, v235
	s_lshl_b32 s14, s15, 13
	v_add_u32_e32 v234, s14, v235
	s_lshl_b32 s14, s15, 6
	v_mov_b32_e32 v232, s14
	v_mov_b32_e32 v233, 0
.LBB0_962:
	s_ashr_i32 s14, s30, 11
	s_ashr_i32 s15, s14, 31
	s_ashr_i32 s31, s30, 31
	s_lshl_b64 s[34:35], s[14:15], 13
	s_lshl_b64 s[14:15], s[30:31], 15
	s_lshl_b64 s[36:37], s[30:31], 14
	v_lshl_add_u64 v[2:3], v[150:151], 0, s[14:15]
	v_mov_b32_e32 v157, v97
	v_lshl_add_u64 v[0:1], v[148:149], 0, s[36:37]
	v_lshl_add_u64 v[4:5], v[2:3], 0, v[96:97]
	v_lshl_add_u64 v[6:7], v[2:3], 0, v[156:157]
	v_mov_b32_e32 v159, v97
	v_lshl_add_u64 v[4:5], v[4:5], 0, v[232:233]
	v_lshl_add_u64 v[238:239], v[2:3], 0, v[232:233]
	global_load_dwordx4 v[24:27], v[4:5], off
	global_load_dwordx4 v[28:31], v[4:5], off offset:1024
	global_load_dwordx4 v[32:35], v[4:5], off offset:2048
	global_load_dwordx4 v[36:39], v[4:5], off offset:3072
	v_lshl_add_u64 v[6:7], v[238:239], 0, v[156:157]
	global_load_dwordx4 v[40:43], v[6:7], off
	v_mov_b32_e32 v161, v97
	v_lshl_add_u64 v[6:7], v[238:239], 0, v[158:159]
	global_load_dwordx4 v[48:51], v[6:7], off
	v_mov_b32_e32 v175, v97
	v_lshl_add_u64 v[6:7], v[238:239], 0, v[160:161]
	global_load_dwordx4 v[56:59], v[6:7], off
	v_lshl_add_u64 v[6:7], v[238:239], 0, v[174:175]
	global_load_dwordx4 v[68:71], v[6:7], off
	global_load_dwordx4 v[12:15], v[0:1], off
	global_load_dwordx4 v[60:63], v[0:1], off offset:64
	global_load_dwordx4 v[64:67], v[0:1], off offset:128
	global_load_dwordx4 v[102:105], v[0:1], off offset:192
	s_and_b32 s9, s5, 0x1fc0
	s_or_b32 s9, s34, s9
	v_or_b32_e32 v178, s9, v146
	v_mov_b64_e32 v[2:3], s[0:1]
	s_and_b32 s10, s30, 0x780
	v_mad_u64_u32 v[2:3], s[14:15], v178, s90, v[2:3]
	v_mad_i32_i24 v3, s35, v226, v3
	s_lshl_b32 s74, s10, 1
	v_lshl_add_u64 v[2:3], v[2:3], 0, s[74:75]
	v_mov_b32_e32 v177, v97
	v_lshl_add_u64 v[0:1], v[152:153], 0, s[36:37]
	v_lshl_add_u64 v[2:3], v[2:3], 0, v[176:177]
	s_mov_b32 s9, 0x22aaf000
	global_load_dwordx4 v[4:7], v[0:1], off
	global_load_dwordx4 v[16:19], v[0:1], off offset:16
	global_load_dwordx4 v[44:47], v[0:1], off offset:32
	global_load_dwordx4 v[142:145], v[0:1], off offset:48
	v_add_co_u32_e32 v0, vcc, s9, v2
	s_mov_b64 s[14:15], 0x22aaf000
	s_nop 0
	v_addc_co_u32_e32 v1, vcc, 0, v3, vcc
	v_lshl_add_u64 v[212:213], v[2:3], 0, s[14:15]
	global_load_dwordx4 v[8:11], v[0:1], off
	global_load_dwordx4 v[20:23], v[212:213], off offset:16
	global_load_dwordx4 v[52:55], v[212:213], off offset:32
	s_nop 0
	global_load_dwordx4 v[0:3], v[212:213], off offset:48
	v_mov_b32_e32 v179, s35
	s_add_i32 s8, s8, s2
	s_add_i32 s30, s30, s4
	s_add_i32 s5, s5, s7
	s_cmpk_lt_i32 s8, 0x800
	s_waitcnt vmcnt(12)
	ds_write_b128 v234, v[24:27] offset:0
	ds_write_b128 v234, v[28:31] offset:1024
	ds_write_b128 v234, v[32:35] offset:2048
	ds_write_b128 v234, v[36:39] offset:3072
	ds_write_b128 v234, v[40:43] offset:4096
	ds_write_b128 v234, v[48:51] offset:5120
	ds_write_b128 v234, v[56:59] offset:6144
	ds_write_b128 v234, v[68:71] offset:7168
	s_waitcnt lgkmcnt(0)
	s_barrier
	ds_read_b128 v[24:27], v235 offset:0
	ds_read_b128 v[28:31], v235 offset:1024
	ds_read_b128 v[32:35], v235 offset:2048
	ds_read_b128 v[36:39], v235 offset:3072
	ds_read_b128 v[40:43], v235 offset:4096
	ds_read_b128 v[48:51], v235 offset:5120
	ds_read_b128 v[56:59], v235 offset:6144
	ds_read_b128 v[68:71], v235 offset:7168
	ds_read_b128 v[72:75], v235 offset:8192
	ds_read_b128 v[76:79], v235 offset:9216
	ds_read_b128 v[80:83], v235 offset:10240
	ds_read_b128 v[84:87], v235 offset:11264
	ds_read_b128 v[88:91], v235 offset:12288
	ds_read_b128 v[92:95], v235 offset:13312
	ds_read_b128 v[98:101], v235 offset:14336
	ds_read_b128 v[106:109], v235 offset:15360
	ds_read_b128 v[110:113], v235 offset:16384
	ds_read_b128 v[114:117], v235 offset:17408
	ds_read_b128 v[118:121], v235 offset:18432
	ds_read_b128 v[122:125], v235 offset:19456
	ds_read_b128 v[126:129], v235 offset:20480
	ds_read_b128 v[130:133], v235 offset:21504
	ds_read_b128 v[134:137], v235 offset:22528
	ds_read_b128 v[138:141], v235 offset:23552
	ds_read_b128 v[180:183], v235 offset:24576
	ds_read_b128 v[184:187], v235 offset:25600
	ds_read_b128 v[188:191], v235 offset:26624
	ds_read_b128 v[192:195], v235 offset:27648
	ds_read_b128 v[196:199], v235 offset:28672
	ds_read_b128 v[200:203], v235 offset:29696
	ds_read_b128 v[206:209], v235 offset:30720
	ds_read_b128 v[228:231], v235 offset:31744
	s_waitcnt vmcnt(0) lgkmcnt(0)
	s_barrier
	s_waitcnt vmcnt(42)
	v_mfma_f32_16x16x32_bf16 v[24:27], v[24:27], v[12:15], 0
	s_waitcnt vmcnt(41)
	v_mfma_f32_16x16x32_bf16 v[28:31], v[28:31], v[12:15], 0
	s_waitcnt vmcnt(40)
	v_mfma_f32_16x16x32_bf16 v[32:35], v[32:35], v[12:15], 0
	s_waitcnt vmcnt(39)
	v_mfma_f32_16x16x32_bf16 v[36:39], v[36:39], v[12:15], 0
	s_waitcnt vmcnt(38)
	v_mfma_f32_16x16x32_bf16 v[40:43], v[40:43], v[12:15], 0
	s_waitcnt vmcnt(37)
	v_mfma_f32_16x16x32_bf16 v[48:51], v[48:51], v[12:15], 0
	s_waitcnt vmcnt(36)
	v_mfma_f32_16x16x32_bf16 v[56:59], v[56:59], v[12:15], 0
	s_waitcnt vmcnt(35)
	v_mfma_f32_16x16x32_bf16 v[12:15], v[68:71], v[12:15], 0
	s_waitcnt vmcnt(33)
	v_mfma_f32_16x16x32_bf16 v[24:27], v[72:75], v[60:63], v[24:27]
	s_waitcnt vmcnt(32)
	v_mfma_f32_16x16x32_bf16 v[28:31], v[76:79], v[60:63], v[28:31]
	s_waitcnt vmcnt(31)
	v_mfma_f32_16x16x32_bf16 v[32:35], v[80:83], v[60:63], v[32:35]
	s_waitcnt vmcnt(30)
	v_mfma_f32_16x16x32_bf16 v[36:39], v[84:87], v[60:63], v[36:39]
	s_waitcnt vmcnt(4)
	v_lshlrev_b32_e32 v84, 16, v145
	v_mfma_f32_16x16x32_bf16 v[40:43], v[88:91], v[60:63], v[40:43]
	v_and_b32_e32 v85, 0xffff0000, v145
	v_mfma_f32_16x16x32_bf16 v[48:51], v[92:95], v[60:63], v[48:51]
	s_waitcnt vmcnt(0)
	v_lshlrev_b32_e32 v92, 16, v1
	v_and_b32_e32 v93, 0xffff0000, v1
	v_mfma_f32_16x16x32_bf16 v[56:59], v[98:101], v[60:63], v[56:59]
	v_mul_f32_e32 v1, 0xbfb8aa3b, v92
	v_exp_f32_e32 v1, v1
	v_mfma_f32_16x16x32_bf16 v[12:15], v[106:109], v[60:63], v[12:15]
	v_lshlrev_b32_e32 v108, 16, v21
	v_add_f32_e32 v1, 1.0, v1
	v_rcp_f32_e32 v94, v1
	v_mfma_f32_16x16x32_bf16 v[24:27], v[110:113], v[64:67], v[24:27]
	v_mul_f32_e32 v1, 0xbfb8aa3b, v93
	v_exp_f32_e32 v1, v1
	v_and_b32_e32 v109, 0xffff0000, v21
	v_mfma_f32_16x16x32_bf16 v[28:31], v[114:117], v[64:67], v[28:31]
	v_lshlrev_b32_e32 v112, 16, v11
	v_add_f32_e32 v1, 1.0, v1
	v_rcp_f32_e32 v95, v1
	v_mfma_f32_16x16x32_bf16 v[32:35], v[118:121], v[64:67], v[32:35]
	v_and_b32_e32 v113, 0xffff0000, v11
	v_lshlrev_b32_e32 v116, 16, v9
	v_pk_mul_f32 v[92:93], v[94:95], v[92:93]
	v_mfma_f32_16x16x32_bf16 v[36:39], v[122:125], v[64:67], v[36:39]
	v_lshlrev_b32_e32 v94, 16, v142
	v_and_b32_e32 v95, 0xffff0000, v142
	v_and_b32_e32 v117, 0xffff0000, v9
	v_mfma_f32_16x16x32_bf16 v[60:63], v[126:129], v[64:67], v[40:43]
	v_mfma_f32_16x16x32_bf16 v[48:51], v[130:133], v[64:67], v[48:51]
	v_mfma_f32_16x16x32_bf16 v[56:59], v[134:137], v[64:67], v[56:59]
	v_mfma_f32_16x16x32_bf16 v[64:67], v[138:141], v[64:67], v[12:15]
	v_mfma_f32_16x16x32_bf16 v[86:89], v[228:231], v[102:105], v[64:67]
	v_mfma_f32_16x16x32_bf16 v[98:101], v[206:209], v[102:105], v[56:59]
	v_mfma_f32_16x16x32_bf16 v[12:15], v[180:183], v[102:105], v[24:27]
	s_nop 5
	v_add_f32_e64 v84, v88, v84
	v_add_f32_e64 v85, v89, v85
	v_lshlrev_b32_e32 v88, 16, v144
	v_and_b32_e32 v89, 0xffff0000, v144
	v_pk_add_f32 v[86:87], v[86:87], v[88:89]
	v_lshlrev_b32_e32 v88, 16, v2
	v_and_b32_e32 v89, 0xffff0000, v2
	v_mul_f32_e32 v2, 0xbfb8aa3b, v88
	v_exp_f32_e32 v2, v2
	v_pk_add_f32 v[94:95], v[98:99], v[94:95]
	v_lshlrev_b32_e32 v98, 16, v0
	v_and_b32_e32 v99, 0xffff0000, v0
	v_add_f32_e32 v2, 1.0, v2
	v_rcp_f32_e32 v90, v2
	v_mul_f32_e32 v2, 0xbfb8aa3b, v89
	v_exp_f32_e32 v2, v2
	v_mul_f32_e32 v0, 0xbfb8aa3b, v98
	v_mul_f32_e32 v1, 0xbfb8aa3b, v99
	v_exp_f32_e32 v0, v0
	v_exp_f32_e32 v1, v1
	v_add_f32_e32 v2, 1.0, v2
	v_rcp_f32_e32 v91, v2
	v_add_f32_e32 v0, 1.0, v0
	v_add_f32_e32 v1, 1.0, v1
	v_rcp_f32_e32 v0, v0
	v_rcp_f32_e32 v1, v1
	v_mfma_f32_16x16x32_bf16 v[24:27], v[184:187], v[102:105], v[28:31]
	v_mul_f32_e64 v88, v90, v88
	v_mul_f32_e64 v89, v91, v89
	v_lshlrev_b32_e32 v90, 16, v143
	v_and_b32_e32 v91, 0xffff0000, v143
	v_mfma_f32_16x16x32_bf16 v[28:31], v[188:191], v[102:105], v[32:35]
	v_add_f32_e64 v90, v100, v90
	v_add_f32_e64 v91, v101, v91
	v_pk_mul_f32 v[0:1], v[0:1], v[98:99]
	v_mov_b32_e32 v98, v90
	v_mfma_f32_16x16x32_bf16 v[40:43], v[192:195], v[102:105], v[36:39]
	v_mov_b32_e32 v99, v84
	v_mov_b32_e32 v100, v91
	v_mov_b32_e32 v101, v85
	v_mfma_f32_16x16x32_bf16 v[72:75], v[196:199], v[102:105], v[60:63]
	v_mfma_f32_16x16x32_bf16 v[80:83], v[200:203], v[102:105], v[48:51]
	v_mov_b32_e32 v104, v95
	v_mov_b32_e32 v105, v87
	v_mov_b32_e32 v102, v94
	v_mov_b32_e32 v103, v86
	v_pk_mul_f32 v[104:105], v[104:105], v[104:105]
	global_load_dwordx4 v[60:63], v[154:155], off offset:48
	global_load_dwordx4 v[64:67], v[154:155], off offset:32
	global_load_dwordx4 v[68:71], v[154:155], off offset:16
	global_load_dwordx4 v[76:79], v[154:155], off
	global_load_dwordx4 v[32:35], v[154:155], off offset:112
	global_load_dwordx4 v[36:39], v[154:155], off offset:96
	global_load_dwordx4 v[48:51], v[154:155], off offset:80
	global_load_dwordx4 v[56:59], v[154:155], off offset:64
	v_pk_fma_f32 v[102:103], v[102:103], v[102:103], v[104:105]
	s_nop 0
	v_pk_fma_f32 v[98:99], v[98:99], v[98:99], v[102:103]
	s_nop 0
	v_pk_fma_f32 v[98:99], v[100:101], v[100:101], v[98:99]
	v_lshlrev_b32_e32 v100, 16, v47
	v_and_b32_e32 v101, 0xffff0000, v47
	v_pk_add_f32 v[82:83], v[82:83], v[100:101]
	v_lshlrev_b32_e32 v100, 16, v55
	v_mul_f32_e32 v2, 0xbfb8aa3b, v100
	v_exp_f32_e32 v2, v2
	v_and_b32_e32 v101, 0xffff0000, v55
	v_add_f32_e32 v2, 1.0, v2
	v_rcp_f32_e32 v102, v2
	v_mul_f32_e32 v2, 0xbfb8aa3b, v101
	v_exp_f32_e32 v2, v2
	s_nop 0
	v_add_f32_e32 v2, 1.0, v2
	v_rcp_f32_e32 v103, v2
	s_nop 0
	v_pk_mul_f32 v[100:101], v[102:103], v[100:101]
	v_lshlrev_b32_e32 v102, 16, v46
	v_and_b32_e32 v103, 0xffff0000, v46
	v_pk_add_f32 v[46:47], v[80:81], v[102:103]
	v_lshlrev_b32_e32 v80, 16, v54
	v_mul_f32_e32 v2, 0xbfb8aa3b, v80
	v_exp_f32_e32 v2, v2
	v_and_b32_e32 v81, 0xffff0000, v54
	v_mov_b32_e32 v107, v47
	v_mov_b32_e32 v105, v46
	v_add_f32_e32 v2, 1.0, v2
	v_rcp_f32_e32 v54, v2
	v_mul_f32_e32 v2, 0xbfb8aa3b, v81
	v_exp_f32_e32 v2, v2
	s_nop 0
	v_add_f32_e32 v2, 1.0, v2
	v_rcp_f32_e32 v55, v2
	s_nop 0
	v_pk_mul_f32 v[54:55], v[54:55], v[80:81]
	v_lshlrev_b32_e32 v80, 16, v45
	v_and_b32_e32 v81, 0xffff0000, v45
	v_pk_add_f32 v[74:75], v[74:75], v[80:81]
	v_lshlrev_b32_e32 v80, 16, v53
	v_mul_f32_e32 v2, 0xbfb8aa3b, v80
	v_exp_f32_e32 v2, v2
	v_and_b32_e32 v81, 0xffff0000, v53
	v_add_f32_e32 v2, 1.0, v2
	v_rcp_f32_e32 v102, v2
	v_mul_f32_e32 v2, 0xbfb8aa3b, v81
	v_exp_f32_e32 v2, v2
	s_nop 0
	v_add_f32_e32 v2, 1.0, v2
	v_rcp_f32_e32 v103, v2
	s_nop 0
	v_pk_mul_f32 v[80:81], v[102:103], v[80:81]
	v_lshlrev_b32_e32 v102, 16, v44
	v_and_b32_e32 v103, 0xffff0000, v44
	v_pk_add_f32 v[44:45], v[72:73], v[102:103]
	v_lshlrev_b32_e32 v72, 16, v52
	v_mul_f32_e32 v2, 0xbfb8aa3b, v72
	v_exp_f32_e32 v2, v2
	v_and_b32_e32 v73, 0xffff0000, v52
	v_mov_b32_e32 v106, v45
	v_mov_b32_e32 v104, v44
	v_add_f32_e32 v2, 1.0, v2
	v_rcp_f32_e32 v52, v2
	v_mul_f32_e32 v2, 0xbfb8aa3b, v73
	v_exp_f32_e32 v2, v2
	v_pk_mul_f32 v[106:107], v[106:107], v[106:107]
	v_mov_b32_e32 v102, v75
	v_pk_fma_f32 v[104:105], v[104:105], v[104:105], v[106:107]
	v_add_f32_e32 v2, 1.0, v2
	v_rcp_f32_e32 v53, v2
	v_mov_b32_e32 v103, v83
	v_pk_mul_f32 v[52:53], v[52:53], v[72:73]
	v_mov_b32_e32 v72, v74
	v_mov_b32_e32 v73, v82
	v_pk_fma_f32 v[72:73], v[72:73], v[72:73], v[104:105]
	v_lshlrev_b32_e32 v104, 16, v23
	v_mul_f32_e32 v2, 0xbfb8aa3b, v104
	v_exp_f32_e32 v2, v2
	v_and_b32_e32 v105, 0xffff0000, v23
	v_pk_fma_f32 v[72:73], v[102:103], v[102:103], v[72:73]
	v_lshlrev_b32_e32 v102, 16, v19
	v_add_f32_e32 v2, 1.0, v2
	v_rcp_f32_e32 v106, v2
	v_mul_f32_e32 v2, 0xbfb8aa3b, v105
	v_exp_f32_e32 v2, v2
	v_and_b32_e32 v103, 0xffff0000, v19
	v_pk_add_f32 v[42:43], v[42:43], v[102:103]
	v_add_f32_e32 v2, 1.0, v2
	v_rcp_f32_e32 v107, v2
	v_pk_mul_f32 v[102:103], v[42:43], v[42:43]
	v_pk_mul_f32 v[104:105], v[106:107], v[104:105]
	v_lshlrev_b32_e32 v106, 16, v18
	v_and_b32_e32 v107, 0xffff0000, v18
	v_pk_add_f32 v[18:19], v[40:41], v[106:107]
	v_lshlrev_b32_e32 v106, 16, v22
	v_mul_f32_e32 v2, 0xbfb8aa3b, v106
	v_exp_f32_e32 v2, v2
	v_and_b32_e32 v107, 0xffff0000, v22
	v_pk_mul_f32 v[40:41], v[18:19], v[18:19]
	v_add_f32_e32 v2, 1.0, v2
	v_rcp_f32_e32 v22, v2
	v_mul_f32_e32 v2, 0xbfb8aa3b, v107
	v_exp_f32_e32 v2, v2
	s_nop 0
	v_add_f32_e32 v2, 1.0, v2
	v_rcp_f32_e32 v23, v2
	v_mul_f32_e32 v2, 0xbfb8aa3b, v108
	v_exp_f32_e32 v2, v2
	v_pk_mul_f32 v[22:23], v[22:23], v[106:107]
	v_lshlrev_b32_e32 v106, 16, v17
	v_add_f32_e32 v2, 1.0, v2
	v_rcp_f32_e32 v110, v2
	v_mul_f32_e32 v2, 0xbfb8aa3b, v109
	v_exp_f32_e32 v2, v2
	v_and_b32_e32 v107, 0xffff0000, v17
	v_pk_add_f32 v[30:31], v[30:31], v[106:107]
	v_add_f32_e32 v2, 1.0, v2
	v_rcp_f32_e32 v111, v2
	v_pk_mul_f32 v[106:107], v[30:31], v[30:31]
	v_pk_mul_f32 v[108:109], v[110:111], v[108:109]
	v_lshlrev_b32_e32 v110, 16, v16
	v_and_b32_e32 v111, 0xffff0000, v16
	v_pk_add_f32 v[16:17], v[28:29], v[110:111]
	v_lshlrev_b32_e32 v110, 16, v20
	v_mul_f32_e32 v2, 0xbfb8aa3b, v110
	v_exp_f32_e32 v2, v2
	v_and_b32_e32 v111, 0xffff0000, v20
	v_pk_mul_f32 v[28:29], v[16:17], v[16:17]
	v_add_f32_e32 v2, 1.0, v2
	v_rcp_f32_e32 v20, v2
	v_mul_f32_e32 v2, 0xbfb8aa3b, v111
	v_exp_f32_e32 v2, v2
	s_nop 0
	v_add_f32_e32 v2, 1.0, v2
	v_rcp_f32_e32 v21, v2
	v_mul_f32_e32 v2, 0xbfb8aa3b, v112
	v_exp_f32_e32 v2, v2
	v_pk_mul_f32 v[20:21], v[20:21], v[110:111]
	v_lshlrev_b32_e32 v110, 16, v7
	v_add_f32_e32 v2, 1.0, v2
	v_rcp_f32_e32 v114, v2
	v_mul_f32_e32 v2, 0xbfb8aa3b, v113
	v_exp_f32_e32 v2, v2
	v_and_b32_e32 v111, 0xffff0000, v7
	v_pk_add_f32 v[26:27], v[26:27], v[110:111]
	v_add_f32_e32 v2, 1.0, v2
	v_rcp_f32_e32 v115, v2
	v_pk_mul_f32 v[110:111], v[26:27], v[26:27]
	v_pk_mul_f32 v[112:113], v[114:115], v[112:113]
	v_lshlrev_b32_e32 v114, 16, v6
	v_and_b32_e32 v115, 0xffff0000, v6
	v_pk_add_f32 v[6:7], v[24:25], v[114:115]
	v_lshlrev_b32_e32 v114, 16, v10
	v_mul_f32_e32 v2, 0xbfb8aa3b, v114
	v_exp_f32_e32 v2, v2
	v_and_b32_e32 v115, 0xffff0000, v10
	v_pk_mul_f32 v[24:25], v[6:7], v[6:7]
	v_add_f32_e32 v2, 1.0, v2
	v_rcp_f32_e32 v10, v2
	v_mul_f32_e32 v2, 0xbfb8aa3b, v115
	v_exp_f32_e32 v2, v2
	s_nop 0
	v_add_f32_e32 v2, 1.0, v2
	v_rcp_f32_e32 v11, v2
	v_mul_f32_e32 v2, 0xbfb8aa3b, v116
	v_exp_f32_e32 v2, v2
	v_pk_mul_f32 v[10:11], v[10:11], v[114:115]
	v_lshlrev_b32_e32 v114, 16, v5
	v_add_f32_e32 v2, 1.0, v2
	v_rcp_f32_e32 v118, v2
	v_mul_f32_e32 v2, 0xbfb8aa3b, v117
	v_exp_f32_e32 v2, v2
	v_and_b32_e32 v115, 0xffff0000, v5
	v_pk_add_f32 v[14:15], v[14:15], v[114:115]
	v_add_f32_e32 v2, 1.0, v2
	v_rcp_f32_e32 v119, v2
	v_pk_mul_f32 v[114:115], v[14:15], v[14:15]
	v_pk_mul_f32 v[116:117], v[118:119], v[116:117]
	v_lshlrev_b32_e32 v118, 16, v4
	v_and_b32_e32 v119, 0xffff0000, v4
	v_pk_add_f32 v[4:5], v[12:13], v[118:119]
	v_lshlrev_b32_e32 v118, 16, v8
	v_mul_f32_e32 v2, 0xbfb8aa3b, v118
	v_exp_f32_e32 v2, v2
	v_and_b32_e32 v119, 0xffff0000, v8
	v_pk_mul_f32 v[12:13], v[4:5], v[4:5]
	v_add_f32_e32 v2, 1.0, v2
	v_rcp_f32_e32 v8, v2
	v_mul_f32_e32 v2, 0xbfb8aa3b, v119
	v_exp_f32_e32 v2, v2
	v_add_f32_e32 v12, v12, v13
	v_add_f32_e32 v12, v114, v12
	v_add_f32_e32 v12, v115, v12
	v_add_f32_e32 v2, 1.0, v2
	v_rcp_f32_e32 v9, v2
	v_add_f32_e32 v2, v24, v25
	v_add_f32_e32 v2, v110, v2
	v_add_f32_e32 v2, v111, v2
	v_add_f32_e32 v2, v12, v2
	v_add_f32_e32 v12, v28, v29
	v_add_f32_e32 v12, v106, v12
	v_add_f32_e32 v12, v107, v12
	v_add_f32_e32 v2, v2, v12
	v_add_f32_e32 v12, v40, v41
	v_add_f32_e32 v12, v102, v12
	v_add_f32_e32 v12, v103, v12
	v_add_f32_e32 v2, v2, v12
	v_add_f32_e32 v2, v2, v72
	v_add_f32_e32 v2, v2, v73
	v_add_f32_e32 v2, v2, v98
	v_add_f32_e32 v2, v2, v99
	ds_swizzle_b32 v12, v2 offset:swizzle(SWAP,16)
	v_pk_mul_f32 v[8:9], v[8:9], v[118:119]
	s_waitcnt lgkmcnt(0)
	v_add_f32_e32 v2, v2, v12
	v_mov_b32_e32 v12, v2
	s_nop 1
	v_permlane32_swap_b32_e32 v2, v12
	v_add_f32_e32 v2, v2, v12
	v_fmamk_f32 v2, v2, 0x3c000000, v205
	v_cmp_gt_f32_e32 vcc, s17, v2
	v_mul_f32_e32 v12, 0x4b800000, v2
	s_nop 0
	v_cndmask_b32_e32 v2, v2, v12, vcc
	v_rsq_f32_e32 v2, v2
	s_nop 0
	v_mul_f32_e32 v12, 0x45800000, v2
	v_cndmask_b32_e32 v2, v2, v12, vcc
	v_pk_mul_f32 v[4:5], v[4:5], v[2:3] op_sel_hi:[1,0]
	v_pk_mul_f32 v[6:7], v[6:7], v[2:3] op_sel_hi:[1,0]
	s_waitcnt vmcnt(4)
	v_pk_mul_f32 v[4:5], v[76:77], v[4:5]
	v_pk_mul_f32 v[6:7], v[68:69], v[6:7]
	v_pk_mul_f32 v[4:5], v[8:9], v[4:5]
	v_pk_mul_f32 v[8:9], v[14:15], v[2:3] op_sel_hi:[1,0]
	v_cvt_pk_bf16_f32 v4, v4, v5
	v_pk_mul_f32 v[8:9], v[78:79], v[8:9]
	v_pk_mul_f32 v[6:7], v[10:11], v[6:7]
	v_pk_mul_f32 v[8:9], v[116:117], v[8:9]
	v_cvt_pk_bf16_f32 v6, v6, v7
	v_cvt_pk_bf16_f32 v5, v8, v9
	v_pk_mul_f32 v[8:9], v[26:27], v[2:3] op_sel_hi:[1,0]
	v_pk_mul_f32 v[10:11], v[30:31], v[2:3] op_sel_hi:[1,0]
	v_pk_mul_f32 v[8:9], v[70:71], v[8:9]
	v_pk_mul_f32 v[10:11], v[66:67], v[10:11]
	v_pk_mul_f32 v[8:9], v[112:113], v[8:9]
	v_pk_mul_f32 v[10:11], v[108:109], v[10:11]
	v_cvt_pk_bf16_f32 v7, v8, v9
	v_pk_mul_f32 v[8:9], v[16:17], v[2:3] op_sel_hi:[1,0]
	v_pk_mul_f32 v[12:13], v[42:43], v[2:3] op_sel_hi:[1,0]
	v_pk_mul_f32 v[8:9], v[64:65], v[8:9]
	v_pk_mul_f32 v[12:13], v[62:63], v[12:13]
	v_pk_mul_f32 v[8:9], v[20:21], v[8:9]
	v_pk_mul_f32 v[12:13], v[104:105], v[12:13]
	v_cvt_pk_bf16_f32 v8, v8, v9
	v_cvt_pk_bf16_f32 v9, v10, v11
	v_pk_mul_f32 v[10:11], v[18:19], v[2:3] op_sel_hi:[1,0]
	v_pk_mul_f32 v[14:15], v[74:75], v[2:3] op_sel_hi:[1,0]
	v_pk_mul_f32 v[10:11], v[60:61], v[10:11]
	s_waitcnt vmcnt(0)
	v_pk_mul_f32 v[14:15], v[58:59], v[14:15]
	v_pk_mul_f32 v[10:11], v[22:23], v[10:11]
	v_pk_mul_f32 v[14:15], v[80:81], v[14:15]
	v_cvt_pk_bf16_f32 v10, v10, v11
	v_cvt_pk_bf16_f32 v11, v12, v13
	v_pk_mul_f32 v[12:13], v[44:45], v[2:3] op_sel_hi:[1,0]
	v_pk_mul_f32 v[16:17], v[82:83], v[2:3] op_sel_hi:[1,0]
	v_pk_mul_f32 v[12:13], v[56:57], v[12:13]
	v_pk_mul_f32 v[16:17], v[50:51], v[16:17]
	v_pk_mul_f32 v[12:13], v[52:53], v[12:13]
	v_pk_mul_f32 v[16:17], v[100:101], v[16:17]
	v_cvt_pk_bf16_f32 v12, v12, v13
	v_cvt_pk_bf16_f32 v13, v14, v15
	v_pk_mul_f32 v[14:15], v[46:47], v[2:3] op_sel_hi:[1,0]
	v_lshlrev_b32_e32 v18, 16, v3
	v_pk_mul_f32 v[14:15], v[48:49], v[14:15]
	v_and_b32_e32 v19, 0xffff0000, v3
	v_pk_mul_f32 v[14:15], v[54:55], v[14:15]
	v_mul_f32_e32 v21, 0xbfb8aa3b, v19
	v_cvt_pk_bf16_f32 v14, v14, v15
	v_cvt_pk_bf16_f32 v15, v16, v17
	v_pk_mul_f32 v[16:17], v[94:95], v[2:3] op_sel_hi:[1,0]
	v_exp_f32_e32 v21, v21
	v_pk_mul_f32 v[16:17], v[36:37], v[16:17]
	v_add_f32_e32 v21, 1.0, v21
	v_pk_mul_f32 v[0:1], v[0:1], v[16:17]
	v_pk_mul_f32 v[16:17], v[90:91], v[2:3] op_sel_hi:[1,0]
	v_cvt_pk_bf16_f32 v0, v0, v1
	v_pk_mul_f32 v[16:17], v[38:39], v[16:17]
	v_rcp_f32_e32 v21, v21
	v_pk_mul_f32 v[16:17], v[92:93], v[16:17]
	s_nop 0
	v_cvt_pk_bf16_f32 v1, v16, v17
	v_pk_mul_f32 v[16:17], v[86:87], v[2:3] op_sel_hi:[1,0]
	v_mul_f32_e32 v3, 0xbfb8aa3b, v18
	v_exp_f32_e32 v3, v3
	v_pk_mul_f32 v[16:17], v[32:33], v[16:17]
	v_add_f32_e32 v3, 1.0, v3
	v_rcp_f32_e32 v20, v3
	v_pk_mul_f32 v[2:3], v[84:85], v[2:3] op_sel_hi:[1,0]
	v_pk_mul_f32 v[16:17], v[88:89], v[16:17]
	v_pk_mul_f32 v[2:3], v[34:35], v[2:3]
	v_pk_mul_f32 v[18:19], v[20:21], v[18:19]
	s_nop 0
	v_pk_mul_f32 v[18:19], v[18:19], v[2:3]
	v_cvt_pk_bf16_f32 v2, v16, v17
	v_lshlrev_b64 v[16:17], 12, v[178:179]
	v_lshl_add_u64 v[16:17], s[28:29], 0, v[16:17]
	v_lshl_add_u64 v[16:17], v[16:17], 0, s[74:75]
	v_lshl_add_u64 v[16:17], v[16:17], 0, v[176:177]
	v_cvt_pk_bf16_f32 v3, v18, v19
	global_store_dwordx4 v[16:17], v[4:7], off
	global_store_dwordx4 v[16:17], v[8:11], off offset:16
	global_store_dwordx4 v[16:17], v[12:15], off offset:32
	global_store_dwordx4 v[16:17], v[0:3], off offset:48
	s_cbranch_scc1 .LBB0_962
